# Fourier stage A: second half waits only for its eight staged loads (counted ladder vmcnt(39..32)) instead of also draining the first half's 32 output stores
# baseline (speedup 1.0000x reference)
.LBB0_432:
	s_xor_b64 s[8:9], s[10:11], -1
	s_and_b64 vcc, exec, s[8:9]
	s_barrier
	s_cbranch_vccnz .Ldfa_h1
	s_waitcnt vmcnt(7)
	ds_write_b128 v156, v[64:67]
	s_waitcnt vmcnt(6)
	ds_write_b128 v157, v[68:71]
	s_waitcnt vmcnt(5)
	ds_write_b128 v158, v[72:75]
	s_waitcnt vmcnt(4)
	ds_write_b128 v159, v[76:79]
	s_waitcnt vmcnt(3)
	ds_write_b128 v160, v[80:83]
	s_waitcnt vmcnt(2)
	ds_write_b128 v161, v[84:87]
	s_waitcnt vmcnt(1)
	ds_write_b128 v162, v[88:91]
	s_waitcnt vmcnt(0)
	ds_write_b128 v163, v[92:95]
	s_branch .Ldfa_hj
.Ldfa_h1:
	s_waitcnt vmcnt(39)
	ds_write_b128 v156, v[64:67]
	s_waitcnt vmcnt(38)
	ds_write_b128 v157, v[68:71]
	s_waitcnt vmcnt(37)
	ds_write_b128 v158, v[72:75]
	s_waitcnt vmcnt(36)
	ds_write_b128 v159, v[76:79]
	s_waitcnt vmcnt(35)
	ds_write_b128 v160, v[80:83]
	s_waitcnt vmcnt(34)
	ds_write_b128 v161, v[84:87]
	s_waitcnt vmcnt(33)
	ds_write_b128 v162, v[88:91]
	s_waitcnt vmcnt(32)
	ds_write_b128 v163, v[92:95]
.Ldfa_hj:
	s_waitcnt lgkmcnt(0)
	s_barrier
	s_cbranch_vccnz .LBB0_434
	global_load_dwordx4 v[64:67], v[114:115], off
	global_load_dwordx4 v[68:71], v[116:117], off
	global_load_dwordx4 v[72:75], v[118:119], off
	global_load_dwordx4 v[76:79], v[120:121], off
	global_load_dwordx4 v[80:83], v[122:123], off
	global_load_dwordx4 v[84:87], v[124:125], off
	global_load_dwordx4 v[88:91], v[126:127], off
	global_load_dwordx4 v[92:95], v[128:129], off
